# accumulator zeroing in the nine GEMM unit loops done with 64-bit moves (half the instructions)
# baseline (speedup 1.0000x reference)
; template <class Epi, class Sched, bool ALIGN_EPI = false, bool SP2 = false, bool GATHER = false, bool F8 = false>
; __device__ __forceinline__ void gemm_phase(PG8_LAS unsigned char* lds, const Gemm g, const Sched& S, const Epi& E) {
;     ...
;         const bool has_next = S.next(ui + 1, nxt);
;         const char* nA = (has_next && !GATHER) ? (const char*)g.A + (size_t)nxt.pm * tstep : cA; const char* nB = has_next ? (const char*)g.Bt + (size_t)nxt.pn * tstep : cB;
;     ...
; #pragma unroll
;         for (int a = 0; a < 2; ++a)
; #pragma unroll
;             for (int b = 0; b < 2; ++b)
; #pragma unroll
;                 for (int m = 0; m < 4; ++m)
; #pragma unroll
;                     for (int n = 0; n < 2; ++n) acc[a][b][m][n] = (f32x4){0.f, 0.f, 0.f, 0.f};
;         cur = nxt; cA = nA; cB = nB; ++ui;
.LBB0_227:
	s_ashr_i32 s17, s16, 31
	s_lshl_b64 s[18:19], s[16:17], 20
	s_add_u32 s18, s62, s18
	s_addc_u32 s19, s63, s19
	s_and_b64 s[20:21], s[0:1], exec
	s_cselect_b32 s17, s19, s25
	s_cselect_b32 s67, s18, s24
	s_ashr_i32 s15, s14, 31
	s_lshl_b64 s[20:21], s[14:15], 20
	v_readlane_b32 s15, v251, 62
	s_add_u32 s20, s15, s20
	v_readlane_b32 s15, v251, 63
	s_addc_u32 s21, s15, s21
	s_and_b64 s[26:27], s[0:1], exec
	s_cselect_b32 s15, s21, s5
	s_cselect_b32 s68, s20, s4
	s_add_u32 s69, s4, 0x100
	s_addc_u32 s70, s5, 0
	s_mov_b32 s71, -2
	v_mov_b64_e32 v[2:3], 0
	v_mov_b64_e32 v[4:5], 0
	v_mov_b64_e32 v[6:7], 0
	v_mov_b64_e32 v[8:9], 0
	v_mov_b64_e32 v[10:11], 0
	v_mov_b64_e32 v[12:13], 0
	v_mov_b64_e32 v[14:15], 0
	v_mov_b64_e32 v[16:17], 0
	v_mov_b64_e32 v[18:19], 0
	v_mov_b64_e32 v[20:21], 0
	v_mov_b64_e32 v[22:23], 0
	v_mov_b64_e32 v[24:25], 0
	v_mov_b64_e32 v[26:27], 0
	v_mov_b64_e32 v[28:29], 0
	v_mov_b64_e32 v[30:31], 0
	v_mov_b64_e32 v[32:33], 0
	v_mov_b64_e32 v[34:35], 0
	v_mov_b64_e32 v[36:37], 0
	v_mov_b64_e32 v[38:39], 0
	v_mov_b64_e32 v[40:41], 0
	v_mov_b64_e32 v[42:43], 0
	v_mov_b64_e32 v[44:45], 0
	v_mov_b64_e32 v[46:47], 0
	v_mov_b64_e32 v[48:49], 0
	v_mov_b64_e32 v[50:51], 0
	v_mov_b64_e32 v[52:53], 0
	v_mov_b64_e32 v[54:55], 0
	v_mov_b64_e32 v[56:57], 0
	v_mov_b64_e32 v[58:59], 0
	v_mov_b64_e32 v[60:61], 0
	v_mov_b64_e32 v[62:63], 0
	v_mov_b64_e32 v[64:65], 0
	v_mov_b64_e32 v[66:67], 0
	v_mov_b64_e32 v[68:69], 0
	v_mov_b64_e32 v[70:71], 0
	v_mov_b64_e32 v[72:73], 0
	v_mov_b64_e32 v[74:75], 0
	v_mov_b64_e32 v[76:77], 0
	v_mov_b64_e32 v[78:79], 0
	v_mov_b64_e32 v[80:81], 0
	v_mov_b64_e32 v[82:83], 0
	v_mov_b64_e32 v[84:85], 0
	v_mov_b64_e32 v[86:87], 0
	v_mov_b64_e32 v[88:89], 0
	v_mov_b64_e32 v[90:91], 0
	v_mov_b64_e32 v[92:93], 0
	v_mov_b64_e32 v[94:95], 0
	v_mov_b64_e32 v[96:97], 0
	v_mov_b64_e32 v[98:99], 0
	v_mov_b64_e32 v[100:101], 0
	v_mov_b64_e32 v[102:103], 0
	v_mov_b64_e32 v[104:105], 0
	v_mov_b64_e32 v[106:107], 0
	v_mov_b64_e32 v[108:109], 0
	v_mov_b64_e32 v[110:111], 0
	v_mov_b64_e32 v[112:113], 0
	v_mov_b64_e32 v[114:115], 0
	v_mov_b64_e32 v[116:117], 0
	v_mov_b64_e32 v[118:119], 0
	v_mov_b64_e32 v[120:121], 0
	v_mov_b64_e32 v[122:123], 0
	v_mov_b64_e32 v[124:125], 0
	v_mov_b64_e32 v[126:127], 0
	v_mov_b64_e32 v[128:129], 0

; template <class Epi, class Sched, bool ALIGN_EPI = false, bool SP2 = false, bool GATHER = false, bool F8 = false>
; __device__ __forceinline__ void gemm_phase(PG8_LAS unsigned char* lds, const Gemm g, const Sched& S, const Epi& E) {
;     ...
;         const bool has_next = S.next(ui + 1, nxt);
;         const char* nA = (has_next && !GATHER) ? (const char*)g.A + (size_t)nxt.pm * tstep : cA; const char* nB = has_next ? (const char*)g.Bt + (size_t)nxt.pn * tstep : cB;
;     ...
; #pragma unroll
;         for (int a = 0; a < 2; ++a)
; #pragma unroll
;             for (int b = 0; b < 2; ++b)
; #pragma unroll
;                 for (int m = 0; m < 4; ++m)
; #pragma unroll
;                     for (int n = 0; n < 2; ++n) acc[a][b][m][n] = (f32x4){0.f, 0.f, 0.f, 0.f};
;         cur = nxt; cA = nA; cB = nB; ++ui;
.LBB0_381:
	s_ashr_i32 s39, s38, 31
	s_lshl_b64 s[10:11], s[38:39], 20
	s_add_u32 s66, s62, s10
	s_addc_u32 s67, s63, s11
	s_and_b64 s[10:11], s[0:1], exec
	s_cselect_b32 s39, s67, s9
	s_cselect_b32 s89, s66, s8
	s_ashr_i32 s37, s36, 31
	s_lshl_b64 s[10:11], s[36:37], 20
	v_readlane_b32 s34, v250, 0
	s_add_u32 s72, s34, s10
	v_readlane_b32 s10, v250, 1
	s_addc_u32 s73, s10, s11
	s_and_b64 s[10:11], s[0:1], exec
	s_cselect_b32 s37, s73, s5
	s_cselect_b32 s92, s72, s4
	s_add_u32 s93, s4, 0x100
	s_addc_u32 s94, s5, 0
	s_mov_b32 s95, -2
	v_mov_b64_e32 v[2:3], 0
	v_mov_b64_e32 v[4:5], 0
	v_mov_b64_e32 v[6:7], 0
	v_mov_b64_e32 v[8:9], 0
	v_mov_b64_e32 v[10:11], 0
	v_mov_b64_e32 v[12:13], 0
	v_mov_b64_e32 v[14:15], 0
	v_mov_b64_e32 v[16:17], 0
	v_mov_b64_e32 v[18:19], 0
	v_mov_b64_e32 v[20:21], 0
	v_mov_b64_e32 v[22:23], 0
	v_mov_b64_e32 v[24:25], 0
	v_mov_b64_e32 v[26:27], 0
	v_mov_b64_e32 v[28:29], 0
	v_mov_b64_e32 v[30:31], 0
	v_mov_b64_e32 v[32:33], 0
	v_mov_b64_e32 v[34:35], 0
	v_mov_b64_e32 v[36:37], 0
	v_mov_b64_e32 v[38:39], 0
	v_mov_b64_e32 v[40:41], 0
	v_mov_b64_e32 v[42:43], 0
	v_mov_b64_e32 v[44:45], 0
	v_mov_b64_e32 v[46:47], 0
	v_mov_b64_e32 v[48:49], 0
	v_mov_b64_e32 v[50:51], 0
	v_mov_b64_e32 v[52:53], 0
	v_mov_b64_e32 v[54:55], 0
	v_mov_b64_e32 v[56:57], 0
	v_mov_b64_e32 v[58:59], 0
	v_mov_b64_e32 v[60:61], 0
	v_mov_b64_e32 v[62:63], 0
	v_mov_b64_e32 v[64:65], 0
	v_mov_b64_e32 v[66:67], 0
	v_mov_b64_e32 v[68:69], 0
	v_mov_b64_e32 v[70:71], 0
	v_mov_b64_e32 v[72:73], 0
	v_mov_b64_e32 v[74:75], 0
	v_mov_b64_e32 v[76:77], 0
	v_mov_b64_e32 v[78:79], 0
	v_mov_b64_e32 v[80:81], 0
	v_mov_b64_e32 v[82:83], 0
	v_mov_b64_e32 v[84:85], 0
	v_mov_b64_e32 v[86:87], 0
	v_mov_b64_e32 v[88:89], 0
	v_mov_b64_e32 v[90:91], 0
	v_mov_b64_e32 v[92:93], 0
	v_mov_b64_e32 v[94:95], 0
	v_mov_b64_e32 v[96:97], 0
	v_mov_b64_e32 v[98:99], 0
	v_mov_b64_e32 v[100:101], 0
	v_mov_b64_e32 v[102:103], 0
	v_mov_b64_e32 v[104:105], 0
	v_mov_b64_e32 v[106:107], 0
	v_mov_b64_e32 v[108:109], 0
	v_mov_b64_e32 v[110:111], 0
	v_mov_b64_e32 v[112:113], 0
	v_mov_b64_e32 v[114:115], 0
	v_mov_b64_e32 v[116:117], 0
	v_mov_b64_e32 v[118:119], 0
	v_mov_b64_e32 v[120:121], 0
	v_mov_b64_e32 v[122:123], 0
	v_mov_b64_e32 v[124:125], 0
	v_mov_b64_e32 v[126:127], 0
	v_mov_b64_e32 v[128:129], 0

; template <class Epi, class Sched, bool ALIGN_EPI = false, bool SP2 = false, bool GATHER = false, bool F8 = false>
; __device__ __forceinline__ void gemm_phase(PG8_LAS unsigned char* lds, const Gemm g, const Sched& S, const Epi& E) {
;     ...
;         const bool has_next = S.next(ui + 1, nxt);
;         const char* nA = (has_next && !GATHER) ? (const char*)g.A + (size_t)nxt.pm * tstep : cA; const char* nB = has_next ? (const char*)g.Bt + (size_t)nxt.pn * tstep : cB;
;     ...
; #pragma unroll
;         for (int a = 0; a < 2; ++a)
; #pragma unroll
;             for (int b = 0; b < 2; ++b)
; #pragma unroll
;                 for (int m = 0; m < 4; ++m)
; #pragma unroll
;                     for (int n = 0; n < 2; ++n) acc[a][b][m][n] = (f32x4){0.f, 0.f, 0.f, 0.f};
;         cur = nxt; cA = nA; cB = nB; ++ui;
.LBB0_493:
	s_ashr_i32 s17, s16, 31
	s_lshl_b64 s[18:19], s[16:17], 20
	v_readlane_b32 s12, v251, 38
	v_readlane_b32 s13, v251, 39
	s_add_u32 s18, s12, s18
	s_addc_u32 s19, s13, s19
	s_and_b64 s[20:21], s[0:1], exec
	s_cselect_b32 s17, s19, s25
	s_cselect_b32 s72, s18, s24
	s_ashr_i32 s15, s14, 31
	s_lshl_b64 s[20:21], s[14:15], 20
	v_readlane_b32 s12, v250, 2
	s_add_u32 s20, s12, s20
	s_addc_u32 s21, s3, s21
	s_and_b64 s[26:27], s[0:1], exec
	s_cselect_b32 s15, s21, s5
	s_cselect_b32 s73, s20, s4
	s_add_u32 s74, s4, 0x100
	s_addc_u32 s75, s5, 0
	s_mov_b32 s76, -2
	v_mov_b64_e32 v[2:3], 0
	v_mov_b64_e32 v[4:5], 0
	v_mov_b64_e32 v[6:7], 0
	v_mov_b64_e32 v[8:9], 0
	v_mov_b64_e32 v[10:11], 0
	v_mov_b64_e32 v[12:13], 0
	v_mov_b64_e32 v[14:15], 0
	v_mov_b64_e32 v[16:17], 0
	v_mov_b64_e32 v[18:19], 0
	v_mov_b64_e32 v[20:21], 0
	v_mov_b64_e32 v[22:23], 0
	v_mov_b64_e32 v[24:25], 0
	v_mov_b64_e32 v[26:27], 0
	v_mov_b64_e32 v[28:29], 0
	v_mov_b64_e32 v[30:31], 0
	v_mov_b64_e32 v[32:33], 0
	v_mov_b64_e32 v[34:35], 0
	v_mov_b64_e32 v[36:37], 0
	v_mov_b64_e32 v[38:39], 0
	v_mov_b64_e32 v[40:41], 0
	v_mov_b64_e32 v[42:43], 0
	v_mov_b64_e32 v[44:45], 0
	v_mov_b64_e32 v[46:47], 0
	v_mov_b64_e32 v[48:49], 0
	v_mov_b64_e32 v[50:51], 0
	v_mov_b64_e32 v[52:53], 0
	v_mov_b64_e32 v[54:55], 0
	v_mov_b64_e32 v[56:57], 0
	v_mov_b64_e32 v[58:59], 0
	v_mov_b64_e32 v[60:61], 0
	v_mov_b64_e32 v[62:63], 0
	v_mov_b64_e32 v[64:65], 0
	v_mov_b64_e32 v[66:67], 0
	v_mov_b64_e32 v[68:69], 0
	v_mov_b64_e32 v[70:71], 0
	v_mov_b64_e32 v[72:73], 0
	v_mov_b64_e32 v[74:75], 0
	v_mov_b64_e32 v[76:77], 0
	v_mov_b64_e32 v[78:79], 0
	v_mov_b64_e32 v[80:81], 0
	v_mov_b64_e32 v[82:83], 0
	v_mov_b64_e32 v[84:85], 0
	v_mov_b64_e32 v[86:87], 0
	v_mov_b64_e32 v[88:89], 0
	v_mov_b64_e32 v[90:91], 0
	v_mov_b64_e32 v[92:93], 0
	v_mov_b64_e32 v[94:95], 0
	v_mov_b64_e32 v[96:97], 0
	v_mov_b64_e32 v[98:99], 0
	v_mov_b64_e32 v[100:101], 0
	v_mov_b64_e32 v[102:103], 0
	v_mov_b64_e32 v[104:105], 0
	v_mov_b64_e32 v[106:107], 0
	v_mov_b64_e32 v[108:109], 0
	v_mov_b64_e32 v[110:111], 0
	v_mov_b64_e32 v[112:113], 0
	v_mov_b64_e32 v[114:115], 0
	v_mov_b64_e32 v[116:117], 0
	v_mov_b64_e32 v[118:119], 0
	v_mov_b64_e32 v[120:121], 0
	v_mov_b64_e32 v[130:131], 0
	v_mov_b64_e32 v[132:133], 0
	v_mov_b64_e32 v[134:135], 0
	v_mov_b64_e32 v[136:137], 0

; template <class Epi, class Sched, bool ALIGN_EPI = false, bool SP2 = false, bool GATHER = false, bool F8 = false>
; __device__ __forceinline__ void gemm_phase(PG8_LAS unsigned char* lds, const Gemm g, const Sched& S, const Epi& E) {
;     ...
;         const bool has_next = S.next(ui + 1, nxt);
;         const char* nA = (has_next && !GATHER) ? (const char*)g.A + (size_t)nxt.pm * tstep : cA; const char* nB = has_next ? (const char*)g.Bt + (size_t)nxt.pn * tstep : cB;
;     ...
; #pragma unroll
;         for (int a = 0; a < 2; ++a)
; #pragma unroll
;             for (int b = 0; b < 2; ++b)
; #pragma unroll
;                 for (int m = 0; m < 4; ++m)
; #pragma unroll
;                     for (int n = 0; n < 2; ++n) acc[a][b][m][n] = (f32x4){0.f, 0.f, 0.f, 0.f};
;         cur = nxt; cA = nA; cB = nB; ++ui;
.LBB0_840:
	s_ashr_i32 s11, s10, 31
	s_lshl_b64 s[14:15], s[10:11], 19
	v_readlane_b32 s11, v250, 7
	s_add_u32 s14, s11, s14
	v_readlane_b32 s11, v250, 8
	s_addc_u32 s15, s11, s15
	s_and_b64 s[20:21], exec, s[12:13]
	s_cselect_b32 s11, s15, s19
	s_cselect_b32 s59, s14, s18
	s_add_u32 s68, s18, 0x100
	s_addc_u32 s69, s19, 0
	s_mov_b32 s70, -2
	s_mov_b64 s[18:19], s[62:63]
	v_mov_b64_e32 v[66:67], 0
	v_mov_b64_e32 v[68:69], 0
	v_mov_b64_e32 v[70:71], 0
	v_mov_b64_e32 v[72:73], 0
	v_mov_b64_e32 v[74:75], 0
	v_mov_b64_e32 v[76:77], 0
	v_mov_b64_e32 v[78:79], 0
	v_mov_b64_e32 v[80:81], 0
	v_mov_b64_e32 v[82:83], 0
	v_mov_b64_e32 v[84:85], 0
	v_mov_b64_e32 v[86:87], 0
	v_mov_b64_e32 v[88:89], 0
	v_mov_b64_e32 v[90:91], 0
	v_mov_b64_e32 v[92:93], 0
	v_mov_b64_e32 v[94:95], 0
	v_mov_b64_e32 v[96:97], 0
	v_mov_b64_e32 v[98:99], 0
	v_mov_b64_e32 v[100:101], 0
	v_mov_b64_e32 v[102:103], 0
	v_mov_b64_e32 v[104:105], 0
	v_mov_b64_e32 v[106:107], 0
	v_mov_b64_e32 v[108:109], 0
	v_mov_b64_e32 v[110:111], 0
	v_mov_b64_e32 v[112:113], 0
	v_mov_b64_e32 v[114:115], 0
	v_mov_b64_e32 v[116:117], 0
	v_mov_b64_e32 v[118:119], 0
	v_mov_b64_e32 v[120:121], 0
	v_mov_b64_e32 v[122:123], 0
	v_mov_b64_e32 v[124:125], 0
	v_mov_b64_e32 v[126:127], 0
	v_mov_b64_e32 v[128:129], 0
	v_mov_b64_e32 v[130:131], 0
	v_mov_b64_e32 v[132:133], 0
	v_mov_b64_e32 v[134:135], 0
	v_mov_b64_e32 v[136:137], 0
	v_mov_b64_e32 v[138:139], 0
	v_mov_b64_e32 v[140:141], 0
	v_mov_b64_e32 v[142:143], 0
	v_mov_b64_e32 v[144:145], 0
	v_mov_b64_e32 v[146:147], 0
	v_mov_b64_e32 v[148:149], 0
	v_mov_b64_e32 v[150:151], 0
	v_mov_b64_e32 v[152:153], 0
	v_mov_b64_e32 v[154:155], 0
	v_mov_b64_e32 v[156:157], 0
	v_mov_b64_e32 v[158:159], 0
	v_mov_b64_e32 v[160:161], 0
	v_mov_b64_e32 v[162:163], 0
	v_mov_b64_e32 v[164:165], 0
	v_mov_b64_e32 v[166:167], 0
	v_mov_b64_e32 v[168:169], 0
	v_mov_b64_e32 v[170:171], 0
	v_mov_b64_e32 v[172:173], 0
	v_mov_b64_e32 v[174:175], 0
	v_mov_b64_e32 v[176:177], 0
	v_mov_b64_e32 v[178:179], 0
	v_mov_b64_e32 v[180:181], 0
	v_mov_b64_e32 v[182:183], 0
	v_mov_b64_e32 v[184:185], 0
	v_mov_b64_e32 v[186:187], 0
	v_mov_b64_e32 v[188:189], 0
	v_mov_b64_e32 v[190:191], 0
	v_mov_b64_e32 v[192:193], 0
	s_branch .LBB0_842

; template <class Epi, class Sched, bool ALIGN_EPI = false, bool SP2 = false, bool GATHER = false, bool F8 = false>
; __device__ __forceinline__ void gemm_phase(PG8_LAS unsigned char* lds, const Gemm g, const Sched& S, const Epi& E) {
;     ...
;         const bool has_next = S.next(ui + 1, nxt);
;         const char* nA = (has_next && !GATHER) ? (const char*)g.A + (size_t)nxt.pm * tstep : cA; const char* nB = has_next ? (const char*)g.Bt + (size_t)nxt.pn * tstep : cB;
;     ...
; #pragma unroll
;         for (int a = 0; a < 2; ++a)
; #pragma unroll
;             for (int b = 0; b < 2; ++b)
; #pragma unroll
;                 for (int m = 0; m < 4; ++m)
; #pragma unroll
;                     for (int n = 0; n < 2; ++n) acc[a][b][m][n] = (f32x4){0.f, 0.f, 0.f, 0.f};
;         cur = nxt; cA = nA; cB = nB; ++ui;
.LBB0_953:
	s_ashr_i32 s11, s10, 31
	s_lshl_b64 s[14:15], s[10:11], 18
	v_readlane_b32 s11, v250, 10
	s_add_u32 s14, s11, s14
	v_readlane_b32 s11, v250, 11
	s_addc_u32 s15, s11, s15
	s_and_b64 s[20:21], exec, s[12:13]
	s_cselect_b32 s11, s15, s19
	s_cselect_b32 s68, s14, s18
	s_add_u32 s69, s18, 0x100
	s_addc_u32 s70, s19, 0
	s_mov_b32 s71, -2
	s_mov_b64 s[18:19], s[94:95]
	v_mov_b64_e32 v[66:67], 0
	v_mov_b64_e32 v[68:69], 0
	v_mov_b64_e32 v[70:71], 0
	v_mov_b64_e32 v[72:73], 0
	v_mov_b64_e32 v[74:75], 0
	v_mov_b64_e32 v[76:77], 0
	v_mov_b64_e32 v[78:79], 0
	v_mov_b64_e32 v[80:81], 0
	v_mov_b64_e32 v[82:83], 0
	v_mov_b64_e32 v[84:85], 0
	v_mov_b64_e32 v[86:87], 0
	v_mov_b64_e32 v[88:89], 0
	v_mov_b64_e32 v[90:91], 0
	v_mov_b64_e32 v[92:93], 0
	v_mov_b64_e32 v[94:95], 0
	v_mov_b64_e32 v[96:97], 0
	v_mov_b64_e32 v[98:99], 0
	v_mov_b64_e32 v[100:101], 0
	v_mov_b64_e32 v[102:103], 0
	v_mov_b64_e32 v[104:105], 0
	v_mov_b64_e32 v[106:107], 0
	v_mov_b64_e32 v[108:109], 0
	v_mov_b64_e32 v[110:111], 0
	v_mov_b64_e32 v[112:113], 0
	v_mov_b64_e32 v[114:115], 0
	v_mov_b64_e32 v[116:117], 0
	v_mov_b64_e32 v[118:119], 0
	v_mov_b64_e32 v[120:121], 0
	v_mov_b64_e32 v[122:123], 0
	v_mov_b64_e32 v[124:125], 0
	v_mov_b64_e32 v[126:127], 0
	v_mov_b64_e32 v[128:129], 0
	v_mov_b64_e32 v[130:131], 0
	v_mov_b64_e32 v[132:133], 0
	v_mov_b64_e32 v[134:135], 0
	v_mov_b64_e32 v[136:137], 0
	v_mov_b64_e32 v[138:139], 0
	v_mov_b64_e32 v[140:141], 0
	v_mov_b64_e32 v[142:143], 0
	v_mov_b64_e32 v[144:145], 0
	v_mov_b64_e32 v[146:147], 0
	v_mov_b64_e32 v[148:149], 0
	v_mov_b64_e32 v[150:151], 0
	v_mov_b64_e32 v[152:153], 0
	v_mov_b64_e32 v[154:155], 0
	v_mov_b64_e32 v[156:157], 0
	v_mov_b64_e32 v[158:159], 0
	v_mov_b64_e32 v[160:161], 0
	v_mov_b64_e32 v[162:163], 0
	v_mov_b64_e32 v[164:165], 0
	v_mov_b64_e32 v[166:167], 0
	v_mov_b64_e32 v[168:169], 0
	v_mov_b64_e32 v[170:171], 0
	v_mov_b64_e32 v[172:173], 0
	v_mov_b64_e32 v[174:175], 0
	v_mov_b64_e32 v[176:177], 0
	v_mov_b64_e32 v[178:179], 0
	v_mov_b64_e32 v[180:181], 0
	v_mov_b64_e32 v[182:183], 0
	v_mov_b64_e32 v[184:185], 0
	v_mov_b64_e32 v[186:187], 0
	v_mov_b64_e32 v[188:189], 0
	v_mov_b64_e32 v[190:191], 0
	v_mov_b64_e32 v[192:193], 0
	s_branch .LBB0_955

; template <class Epi, class Sched, bool ALIGN_EPI = false, bool SP2 = false, bool GATHER = false, bool F8 = false>
; __device__ __forceinline__ void gemm_phase(PG8_LAS unsigned char* lds, const Gemm g, const Sched& S, const Epi& E) {
;     ...
;         const bool has_next = S.next(ui + 1, nxt);
;         const char* nA = (has_next && !GATHER) ? (const char*)g.A + (size_t)nxt.pm * tstep : cA; const char* nB = has_next ? (const char*)g.Bt + (size_t)nxt.pn * tstep : cB;
;     ...
; #pragma unroll
;         for (int a = 0; a < 2; ++a)
; #pragma unroll
;             for (int b = 0; b < 2; ++b)
; #pragma unroll
;                 for (int m = 0; m < 4; ++m)
; #pragma unroll
;                     for (int n = 0; n < 2; ++n) acc[a][b][m][n] = (f32x4){0.f, 0.f, 0.f, 0.f};
;         cur = nxt; cA = nA; cB = nB; ++ui;
.LBB0_1142:
	s_ashr_i32 s21, s20, 31
	s_lshl_b64 s[24:25], s[20:21], 19
	s_add_u32 s24, s66, s24
	v_readlane_b32 s1, v250, 4
	s_addc_u32 s25, s1, s25
	s_and_b64 s[28:29], exec, s[22:23]
	s_cselect_b32 s1, s25, s27
	s_cselect_b32 s21, s24, s26
	s_add_u32 s88, s26, 0x100
	s_addc_u32 s89, s27, 0
	s_mov_b32 s90, -2
	s_mov_b64 s[26:27], s[62:63]
	v_mov_b64_e32 v[66:67], 0
	v_mov_b64_e32 v[68:69], 0
	v_mov_b64_e32 v[70:71], 0
	v_mov_b64_e32 v[72:73], 0
	v_mov_b64_e32 v[74:75], 0
	v_mov_b64_e32 v[76:77], 0
	v_mov_b64_e32 v[78:79], 0
	v_mov_b64_e32 v[80:81], 0
	v_mov_b64_e32 v[82:83], 0
	v_mov_b64_e32 v[84:85], 0
	v_mov_b64_e32 v[86:87], 0
	v_mov_b64_e32 v[88:89], 0
	v_mov_b64_e32 v[90:91], 0
	v_mov_b64_e32 v[92:93], 0
	v_mov_b64_e32 v[94:95], 0
	v_mov_b64_e32 v[96:97], 0
	v_mov_b64_e32 v[98:99], 0
	v_mov_b64_e32 v[100:101], 0
	v_mov_b64_e32 v[102:103], 0
	v_mov_b64_e32 v[104:105], 0
	v_mov_b64_e32 v[106:107], 0
	v_mov_b64_e32 v[108:109], 0
	v_mov_b64_e32 v[110:111], 0
	v_mov_b64_e32 v[112:113], 0
	v_mov_b64_e32 v[114:115], 0
	v_mov_b64_e32 v[116:117], 0
	v_mov_b64_e32 v[118:119], 0
	v_mov_b64_e32 v[120:121], 0
	v_mov_b64_e32 v[122:123], 0
	v_mov_b64_e32 v[124:125], 0
	v_mov_b64_e32 v[126:127], 0
	v_mov_b64_e32 v[128:129], 0
	v_mov_b64_e32 v[130:131], 0
	v_mov_b64_e32 v[132:133], 0
	v_mov_b64_e32 v[134:135], 0
	v_mov_b64_e32 v[136:137], 0
	v_mov_b64_e32 v[138:139], 0
	v_mov_b64_e32 v[140:141], 0
	v_mov_b64_e32 v[142:143], 0
	v_mov_b64_e32 v[144:145], 0
	v_mov_b64_e32 v[146:147], 0
	v_mov_b64_e32 v[148:149], 0
	v_mov_b64_e32 v[150:151], 0
	v_mov_b64_e32 v[152:153], 0
	v_mov_b64_e32 v[154:155], 0
	v_mov_b64_e32 v[156:157], 0
	v_mov_b64_e32 v[158:159], 0
	v_mov_b64_e32 v[160:161], 0
	v_mov_b64_e32 v[162:163], 0
	v_mov_b64_e32 v[164:165], 0
	v_mov_b64_e32 v[166:167], 0
	v_mov_b64_e32 v[168:169], 0
	v_mov_b64_e32 v[170:171], 0
	v_mov_b64_e32 v[172:173], 0
	v_mov_b64_e32 v[174:175], 0
	v_mov_b64_e32 v[176:177], 0
	v_mov_b64_e32 v[178:179], 0
	v_mov_b64_e32 v[180:181], 0
	v_mov_b64_e32 v[182:183], 0
	v_mov_b64_e32 v[184:185], 0
	v_mov_b64_e32 v[186:187], 0
	v_mov_b64_e32 v[188:189], 0
	v_mov_b64_e32 v[190:191], 0
	v_mov_b64_e32 v[192:193], 0
	s_branch .LBB0_1144

; template <class Epi, class Sched, bool ALIGN_EPI = false, bool SP2 = false, bool GATHER = false, bool F8 = false>
; __device__ __forceinline__ void gemm_phase(PG8_LAS unsigned char* lds, const Gemm g, const Sched& S, const Epi& E) {
;     ...
;         const bool has_next = S.next(ui + 1, nxt);
;         const char* nA = (has_next && !GATHER) ? (const char*)g.A + (size_t)nxt.pm * tstep : cA; const char* nB = has_next ? (const char*)g.Bt + (size_t)nxt.pn * tstep : cB;
;     ...
; #pragma unroll
;         for (int a = 0; a < 2; ++a)
; #pragma unroll
;             for (int b = 0; b < 2; ++b)
; #pragma unroll
;                 for (int m = 0; m < 4; ++m)
; #pragma unroll
;                     for (int n = 0; n < 2; ++n) acc[a][b][m][n] = (f32x4){0.f, 0.f, 0.f, 0.f};
;         cur = nxt; cA = nA; cB = nB; ++ui;
.LBB0_1386:
	s_ashr_i32 s15, s14, 31
	s_lshl_b64 s[16:17], s[14:15], 19
	v_readlane_b32 s15, v250, 5
	s_add_u32 s16, s15, s16
	v_readlane_b32 s15, v250, 6
	s_addc_u32 s17, s15, s17
	s_and_b64 s[20:21], exec, s[0:1]
	s_cselect_b32 s15, s17, s19
	s_cselect_b32 s58, s16, s18
	s_add_u32 s59, s18, 0x100
	s_addc_u32 s64, s19, 0
	s_mov_b32 s65, -2
	s_mov_b64 s[18:19], s[94:95]
	v_mov_b64_e32 v[66:67], 0
	v_mov_b64_e32 v[68:69], 0
	v_mov_b64_e32 v[70:71], 0
	v_mov_b64_e32 v[72:73], 0
	v_mov_b64_e32 v[74:75], 0
	v_mov_b64_e32 v[76:77], 0
	v_mov_b64_e32 v[78:79], 0
	v_mov_b64_e32 v[80:81], 0
	v_mov_b64_e32 v[82:83], 0
	v_mov_b64_e32 v[84:85], 0
	v_mov_b64_e32 v[86:87], 0
	v_mov_b64_e32 v[88:89], 0
	v_mov_b64_e32 v[90:91], 0
	v_mov_b64_e32 v[92:93], 0
	v_mov_b64_e32 v[94:95], 0
	v_mov_b64_e32 v[96:97], 0
	v_mov_b64_e32 v[98:99], 0
	v_mov_b64_e32 v[100:101], 0
	v_mov_b64_e32 v[102:103], 0
	v_mov_b64_e32 v[104:105], 0
	v_mov_b64_e32 v[106:107], 0
	v_mov_b64_e32 v[108:109], 0
	v_mov_b64_e32 v[110:111], 0
	v_mov_b64_e32 v[112:113], 0
	v_mov_b64_e32 v[114:115], 0
	v_mov_b64_e32 v[116:117], 0
	v_mov_b64_e32 v[118:119], 0
	v_mov_b64_e32 v[120:121], 0
	v_mov_b64_e32 v[122:123], 0
	v_mov_b64_e32 v[124:125], 0
	v_mov_b64_e32 v[126:127], 0
	v_mov_b64_e32 v[128:129], 0
	v_mov_b64_e32 v[130:131], 0
	v_mov_b64_e32 v[132:133], 0
	v_mov_b64_e32 v[134:135], 0
	v_mov_b64_e32 v[136:137], 0
	v_mov_b64_e32 v[138:139], 0
	v_mov_b64_e32 v[140:141], 0
	v_mov_b64_e32 v[142:143], 0
	v_mov_b64_e32 v[144:145], 0
	v_mov_b64_e32 v[146:147], 0
	v_mov_b64_e32 v[148:149], 0
	v_mov_b64_e32 v[150:151], 0
	v_mov_b64_e32 v[152:153], 0
	v_mov_b64_e32 v[154:155], 0
	v_mov_b64_e32 v[156:157], 0
	v_mov_b64_e32 v[158:159], 0
	v_mov_b64_e32 v[160:161], 0
	v_mov_b64_e32 v[162:163], 0
	v_mov_b64_e32 v[164:165], 0
	v_mov_b64_e32 v[166:167], 0
	v_mov_b64_e32 v[168:169], 0
	v_mov_b64_e32 v[170:171], 0
	v_mov_b64_e32 v[172:173], 0
	v_mov_b64_e32 v[174:175], 0
	v_mov_b64_e32 v[176:177], 0
	v_mov_b64_e32 v[178:179], 0
	v_mov_b64_e32 v[180:181], 0
	v_mov_b64_e32 v[182:183], 0
	v_mov_b64_e32 v[184:185], 0
	v_mov_b64_e32 v[186:187], 0
	v_mov_b64_e32 v[188:189], 0
	v_mov_b64_e32 v[190:191], 0
	v_mov_b64_e32 v[192:193], 0
	s_branch .LBB0_1388

; template <class Epi, class Sched, bool ALIGN_EPI = false, bool SP2 = false, bool GATHER = false, bool F8 = false>
; __device__ __forceinline__ void gemm_phase(PG8_LAS unsigned char* lds, const Gemm g, const Sched& S, const Epi& E) {
;     ...
;         const bool has_next = S.next(ui + 1, nxt);
;         const char* nA = (has_next && !GATHER) ? (const char*)g.A + (size_t)nxt.pm * tstep : cA; const char* nB = has_next ? (const char*)g.Bt + (size_t)nxt.pn * tstep : cB;
;     ...
; #pragma unroll
;         for (int a = 0; a < 2; ++a)
; #pragma unroll
;             for (int b = 0; b < 2; ++b)
; #pragma unroll
;                 for (int m = 0; m < 4; ++m)
; #pragma unroll
;                     for (int n = 0; n < 2; ++n) acc[a][b][m][n] = (f32x4){0.f, 0.f, 0.f, 0.f};
;         cur = nxt; cA = nA; cB = nB; ++ui;
.LBB0_1887:
	s_ashr_i32 s13, s12, 31
	s_lshl_b64 s[16:17], s[12:13], 19
	s_add_u32 s16, s3, s16
	s_addc_u32 s17, s11, s17
	s_and_b64 s[22:23], exec, s[14:15]
	s_cselect_b32 s13, s17, s21
	s_cselect_b32 s51, s16, s20
	s_add_u32 s52, s20, 0x100
	s_addc_u32 s53, s21, 0
	s_mov_b32 s54, -2
	s_mov_b64 s[20:21], s[62:63]
	v_mov_b64_e32 v[66:67], 0
	v_mov_b64_e32 v[68:69], 0
	v_mov_b64_e32 v[70:71], 0
	v_mov_b64_e32 v[72:73], 0
	v_mov_b64_e32 v[74:75], 0
	v_mov_b64_e32 v[76:77], 0
	v_mov_b64_e32 v[78:79], 0
	v_mov_b64_e32 v[80:81], 0
	v_mov_b64_e32 v[82:83], 0
	v_mov_b64_e32 v[84:85], 0
	v_mov_b64_e32 v[86:87], 0
	v_mov_b64_e32 v[88:89], 0
	v_mov_b64_e32 v[90:91], 0
	v_mov_b64_e32 v[92:93], 0
	v_mov_b64_e32 v[94:95], 0
	v_mov_b64_e32 v[96:97], 0
	v_mov_b64_e32 v[98:99], 0
	v_mov_b64_e32 v[100:101], 0
	v_mov_b64_e32 v[102:103], 0
	v_mov_b64_e32 v[104:105], 0
	v_mov_b64_e32 v[106:107], 0
	v_mov_b64_e32 v[108:109], 0
	v_mov_b64_e32 v[110:111], 0
	v_mov_b64_e32 v[112:113], 0
	v_mov_b64_e32 v[114:115], 0
	v_mov_b64_e32 v[116:117], 0
	v_mov_b64_e32 v[118:119], 0
	v_mov_b64_e32 v[120:121], 0
	v_mov_b64_e32 v[122:123], 0
	v_mov_b64_e32 v[124:125], 0
	v_mov_b64_e32 v[126:127], 0
	v_mov_b64_e32 v[128:129], 0
	v_mov_b64_e32 v[130:131], 0
	v_mov_b64_e32 v[132:133], 0
	v_mov_b64_e32 v[134:135], 0
	v_mov_b64_e32 v[136:137], 0
	v_mov_b64_e32 v[138:139], 0
	v_mov_b64_e32 v[140:141], 0
	v_mov_b64_e32 v[142:143], 0
	v_mov_b64_e32 v[144:145], 0
	v_mov_b64_e32 v[146:147], 0
	v_mov_b64_e32 v[148:149], 0
	v_mov_b64_e32 v[150:151], 0
	v_mov_b64_e32 v[152:153], 0
	v_mov_b64_e32 v[154:155], 0
	v_mov_b64_e32 v[156:157], 0
	v_mov_b64_e32 v[158:159], 0
	v_mov_b64_e32 v[160:161], 0
	v_mov_b64_e32 v[162:163], 0
	v_mov_b64_e32 v[164:165], 0
	v_mov_b64_e32 v[166:167], 0
	v_mov_b64_e32 v[168:169], 0
	v_mov_b64_e32 v[170:171], 0
	v_mov_b64_e32 v[172:173], 0
	v_mov_b64_e32 v[174:175], 0
	v_mov_b64_e32 v[176:177], 0
	v_mov_b64_e32 v[178:179], 0
	v_mov_b64_e32 v[180:181], 0
	v_mov_b64_e32 v[182:183], 0
	v_mov_b64_e32 v[184:185], 0
	v_mov_b64_e32 v[186:187], 0
	v_mov_b64_e32 v[188:189], 0
	v_mov_b64_e32 v[190:191], 0
	v_mov_b64_e32 v[192:193], 0
	s_branch .LBB0_1889

; template <class Epi, class Sched, bool ALIGN_EPI = false, bool SP2 = false, bool GATHER = false, bool F8 = false>
; __device__ __forceinline__ void gemm_phase(PG8_LAS unsigned char* lds, const Gemm g, const Sched& S, const Epi& E) {
;     ...
;         const bool has_next = S.next(ui + 1, nxt);
;         const char* nA = (has_next && !GATHER) ? (const char*)g.A + (size_t)nxt.pm * tstep : cA; const char* nB = has_next ? (const char*)g.Bt + (size_t)nxt.pn * tstep : cB;
;     ...
; #pragma unroll
;         for (int a = 0; a < 2; ++a)
; #pragma unroll
;             for (int b = 0; b < 2; ++b)
; #pragma unroll
;                 for (int m = 0; m < 4; ++m)
; #pragma unroll
;                     for (int n = 0; n < 2; ++n) acc[a][b][m][n] = (f32x4){0.f, 0.f, 0.f, 0.f};
;         cur = nxt; cA = nA; cB = nB; ++ui;
.LBB0_1962:
	s_ashr_i32 s19, s18, 31
	s_lshl_b64 s[22:23], s[18:19], 18
	s_add_u32 s22, s3, s22
	s_addc_u32 s23, s38, s23
	s_and_b64 s[28:29], exec, s[20:21]
	s_cselect_b32 s19, s23, s27
	s_cselect_b32 s59, s22, s26
	s_add_u32 s62, s26, 0x100
	s_addc_u32 s63, s27, 0
	s_mov_b32 s64, -2
	s_mov_b64 s[26:27], s[94:95]
	v_mov_b64_e32 v[66:67], 0
	v_mov_b64_e32 v[68:69], 0
	v_mov_b64_e32 v[70:71], 0
	v_mov_b64_e32 v[72:73], 0
	v_mov_b64_e32 v[74:75], 0
	v_mov_b64_e32 v[76:77], 0
	v_mov_b64_e32 v[78:79], 0
	v_mov_b64_e32 v[80:81], 0
	v_mov_b64_e32 v[82:83], 0
	v_mov_b64_e32 v[84:85], 0
	v_mov_b64_e32 v[86:87], 0
	v_mov_b64_e32 v[88:89], 0
	v_mov_b64_e32 v[90:91], 0
	v_mov_b64_e32 v[92:93], 0
	v_mov_b64_e32 v[94:95], 0
	v_mov_b64_e32 v[96:97], 0
	v_mov_b64_e32 v[98:99], 0
	v_mov_b64_e32 v[100:101], 0
	v_mov_b64_e32 v[102:103], 0
	v_mov_b64_e32 v[104:105], 0
	v_mov_b64_e32 v[106:107], 0
	v_mov_b64_e32 v[108:109], 0
	v_mov_b64_e32 v[110:111], 0
	v_mov_b64_e32 v[112:113], 0
	v_mov_b64_e32 v[114:115], 0
	v_mov_b64_e32 v[116:117], 0
	v_mov_b64_e32 v[118:119], 0
	v_mov_b64_e32 v[120:121], 0
	v_mov_b64_e32 v[122:123], 0
	v_mov_b64_e32 v[124:125], 0
	v_mov_b64_e32 v[126:127], 0
	v_mov_b64_e32 v[128:129], 0
	v_mov_b64_e32 v[130:131], 0
	v_mov_b64_e32 v[132:133], 0
	v_mov_b64_e32 v[134:135], 0
	v_mov_b64_e32 v[136:137], 0
	v_mov_b64_e32 v[138:139], 0
	v_mov_b64_e32 v[140:141], 0
	v_mov_b64_e32 v[142:143], 0
	v_mov_b64_e32 v[144:145], 0
	v_mov_b64_e32 v[146:147], 0
	v_mov_b64_e32 v[148:149], 0
	v_mov_b64_e32 v[150:151], 0
	v_mov_b64_e32 v[152:153], 0
	v_mov_b64_e32 v[154:155], 0
	v_mov_b64_e32 v[156:157], 0
	v_mov_b64_e32 v[158:159], 0
	v_mov_b64_e32 v[160:161], 0
	v_mov_b64_e32 v[162:163], 0
	v_mov_b64_e32 v[164:165], 0
	v_mov_b64_e32 v[166:167], 0
	v_mov_b64_e32 v[168:169], 0
	v_mov_b64_e32 v[170:171], 0
	v_mov_b64_e32 v[172:173], 0
	v_mov_b64_e32 v[174:175], 0
	v_mov_b64_e32 v[176:177], 0
	v_mov_b64_e32 v[178:179], 0
	v_mov_b64_e32 v[180:181], 0
	v_mov_b64_e32 v[182:183], 0
	v_mov_b64_e32 v[184:185], 0
	v_mov_b64_e32 v[186:187], 0
	v_mov_b64_e32 v[188:189], 0
	v_mov_b64_e32 v[190:191], 0
	v_mov_b64_e32 v[192:193], 0
	s_branch .LBB0_1964
